# v49 + hand-written fused phase 2a+2b (f32 means computed on the fly from fp64 sums inside the MFMA loop; one barrier fewer)
# baseline (speedup 1.0000x reference)
.LBB0_118:
	s_waitcnt vmcnt(0) lgkmcnt(0)
	s_barrier
	v_mov_b32_e32 v110, 0x11100
	v_lshl_add_u32 v110, v138, 2, v110
	ds_read_b32 v100, v110
	v_mov_b32_e32 v111, 0x11300
	v_lshl_add_u32 v111, v134, 2, v111
	ds_read_b32 v105, v111
	v_mul_u32_u24_e32 v102, 0x810, v138
	v_lshl_add_u32 v102, v140, 3, v102
	v_mul_u32_u24_e32 v103, 0x408, v138
	v_lshl_add_u32 v103, v140, 2, v103
	ds_read_b64 v[84:85], v102 offset:32768
	ds_read_b64 v[86:87], v102 offset:33280
	ds_read_b64 v[88:89], v102 offset:33792
	ds_read_b64 v[90:91], v102 offset:34304
	ds_read_b64 v[92:93], v102 offset:32800
	ds_read_b64 v[94:95], v102 offset:33312
	ds_read_b64 v[96:97], v102 offset:33824
	ds_read_b64 v[98:99], v102 offset:34336
	v_mov_b32_e32 v104, 0
	s_lshl_b32 s29, s17, 2
	s_waitcnt lgkmcnt(8)
	v_max_i32_e32 v100, 1, v100
	v_cvt_f32_u32_e32 v100, v100
	v_div_scale_f32 v110, s[30:31], v100, v100, 1.0
	v_rcp_f32_e32 v111, v110
	v_div_scale_f32 v112, vcc, 1.0, v100, 1.0
	v_fma_f32 v113, -v110, v111, 1.0
	v_fmac_f32_e32 v111, v113, v111
	v_mul_f32_e32 v113, v112, v111
	v_fma_f32 v114, -v110, v113, v112
	v_fmac_f32_e32 v113, v114, v111
	v_fma_f32 v112, -v110, v113, v112
	v_div_fmas_f32 v114, v112, v111, v113
	v_div_fixup_f32 v101, v114, v100, 1.0
	s_waitcnt lgkmcnt(7)
	v_cvt_f32_f64_e32 v80, v[84:85]
	v_mul_f32_e32 v80, v101, v80
	v_fmac_f32_e32 v104, v80, v80
	ds_write_b32 v103, v80 offset:0
	ds_read_b64 v[84:85], v102 offset:32832
	v_mfma_f32_16x16x4_f32 a[0:3], v80, v62, 0
	s_waitcnt lgkmcnt(8)
	v_cvt_f32_f64_e32 v81, v[86:87]
	v_mul_f32_e32 v81, v101, v81
	v_fmac_f32_e32 v104, v81, v81
	ds_write_b32 v103, v81 offset:256
	ds_read_b64 v[86:87], v102 offset:33344
	v_mfma_f32_16x16x4_f32 a[4:7], v81, v63, 0
	s_waitcnt lgkmcnt(9)
	v_cvt_f32_f64_e32 v82, v[88:89]
	v_mul_f32_e32 v82, v101, v82
	v_fmac_f32_e32 v104, v82, v82
	ds_write_b32 v103, v82 offset:512
	ds_read_b64 v[88:89], v102 offset:33856
	v_mfma_f32_16x16x4_f32 a[0:3], v82, v64, a[0:3]
	s_waitcnt lgkmcnt(10)
	v_cvt_f32_f64_e32 v83, v[90:91]
	v_mul_f32_e32 v83, v101, v83
	v_fmac_f32_e32 v104, v83, v83
	ds_write_b32 v103, v83 offset:768
	ds_read_b64 v[90:91], v102 offset:34368
	v_mfma_f32_16x16x4_f32 a[4:7], v83, v65, a[4:7]
	s_waitcnt lgkmcnt(11)
	v_cvt_f32_f64_e32 v80, v[92:93]
	v_mul_f32_e32 v80, v101, v80
	v_fmac_f32_e32 v104, v80, v80
	ds_write_b32 v103, v80 offset:16
	ds_read_b64 v[92:93], v102 offset:32864
	v_mfma_f32_16x16x4_f32 a[0:3], v80, v58, a[0:3]
	s_waitcnt lgkmcnt(12)
	v_cvt_f32_f64_e32 v81, v[94:95]
	v_mul_f32_e32 v81, v101, v81
	v_fmac_f32_e32 v104, v81, v81
	ds_write_b32 v103, v81 offset:272
	ds_read_b64 v[94:95], v102 offset:33376
	v_mfma_f32_16x16x4_f32 a[4:7], v81, v59, a[4:7]
	s_waitcnt lgkmcnt(13)
	v_cvt_f32_f64_e32 v82, v[96:97]
	v_mul_f32_e32 v82, v101, v82
	v_fmac_f32_e32 v104, v82, v82
	ds_write_b32 v103, v82 offset:528
	ds_read_b64 v[96:97], v102 offset:33888
	v_mfma_f32_16x16x4_f32 a[0:3], v82, v60, a[0:3]
	s_waitcnt lgkmcnt(14)
	v_cvt_f32_f64_e32 v83, v[98:99]
	v_mul_f32_e32 v83, v101, v83
	v_fmac_f32_e32 v104, v83, v83
	ds_write_b32 v103, v83 offset:784
	ds_read_b64 v[98:99], v102 offset:34400
	v_mfma_f32_16x16x4_f32 a[4:7], v83, v61, a[4:7]
	s_waitcnt lgkmcnt(14)
	v_cvt_f32_f64_e32 v80, v[84:85]
	v_mul_f32_e32 v80, v101, v80
	v_fmac_f32_e32 v104, v80, v80
	ds_write_b32 v103, v80 offset:32
	ds_read_b64 v[84:85], v102 offset:32896
	v_mfma_f32_16x16x4_f32 a[0:3], v80, v54, a[0:3]
	s_waitcnt lgkmcnt(14)
	v_cvt_f32_f64_e32 v81, v[86:87]
	v_mul_f32_e32 v81, v101, v81
	v_fmac_f32_e32 v104, v81, v81
	ds_write_b32 v103, v81 offset:288
	ds_read_b64 v[86:87], v102 offset:33408
	v_mfma_f32_16x16x4_f32 a[4:7], v81, v55, a[4:7]
	s_waitcnt lgkmcnt(14)
	v_cvt_f32_f64_e32 v82, v[88:89]
	v_mul_f32_e32 v82, v101, v82
	v_fmac_f32_e32 v104, v82, v82
	ds_write_b32 v103, v82 offset:544
	ds_read_b64 v[88:89], v102 offset:33920
	v_mfma_f32_16x16x4_f32 a[0:3], v82, v56, a[0:3]
	s_waitcnt lgkmcnt(14)
	v_cvt_f32_f64_e32 v83, v[90:91]
	v_mul_f32_e32 v83, v101, v83
	v_fmac_f32_e32 v104, v83, v83
	ds_write_b32 v103, v83 offset:800
	ds_read_b64 v[90:91], v102 offset:34432
	v_mfma_f32_16x16x4_f32 a[4:7], v83, v57, a[4:7]
	s_waitcnt lgkmcnt(14)
	v_cvt_f32_f64_e32 v80, v[92:93]
	v_mul_f32_e32 v80, v101, v80
	v_fmac_f32_e32 v104, v80, v80
	ds_write_b32 v103, v80 offset:48
	ds_read_b64 v[92:93], v102 offset:32928
	v_mfma_f32_16x16x4_f32 a[0:3], v80, v50, a[0:3]
	s_waitcnt lgkmcnt(14)
	v_cvt_f32_f64_e32 v81, v[94:95]
	v_mul_f32_e32 v81, v101, v81
	v_fmac_f32_e32 v104, v81, v81
	ds_write_b32 v103, v81 offset:304
	ds_read_b64 v[94:95], v102 offset:33440
	v_mfma_f32_16x16x4_f32 a[4:7], v81, v51, a[4:7]
	s_waitcnt lgkmcnt(14)
	v_cvt_f32_f64_e32 v82, v[96:97]
	v_mul_f32_e32 v82, v101, v82
	v_fmac_f32_e32 v104, v82, v82
	ds_write_b32 v103, v82 offset:560
	ds_read_b64 v[96:97], v102 offset:33952
	v_mfma_f32_16x16x4_f32 a[0:3], v82, v52, a[0:3]
	s_waitcnt lgkmcnt(14)
	v_cvt_f32_f64_e32 v83, v[98:99]
	v_mul_f32_e32 v83, v101, v83
	v_fmac_f32_e32 v104, v83, v83
	ds_write_b32 v103, v83 offset:816
	ds_read_b64 v[98:99], v102 offset:34464
	v_mfma_f32_16x16x4_f32 a[4:7], v83, v53, a[4:7]
	s_waitcnt lgkmcnt(14)
	v_cvt_f32_f64_e32 v80, v[84:85]
	v_mul_f32_e32 v80, v101, v80
	v_fmac_f32_e32 v104, v80, v80
	ds_write_b32 v103, v80 offset:64
	ds_read_b64 v[84:85], v102 offset:32960
	v_mfma_f32_16x16x4_f32 a[0:3], v80, v46, a[0:3]
	s_waitcnt lgkmcnt(14)
	v_cvt_f32_f64_e32 v81, v[86:87]
	v_mul_f32_e32 v81, v101, v81
	v_fmac_f32_e32 v104, v81, v81
	ds_write_b32 v103, v81 offset:320
	ds_read_b64 v[86:87], v102 offset:33472
	v_mfma_f32_16x16x4_f32 a[4:7], v81, v47, a[4:7]
	s_waitcnt lgkmcnt(14)
	v_cvt_f32_f64_e32 v82, v[88:89]
	v_mul_f32_e32 v82, v101, v82
	v_fmac_f32_e32 v104, v82, v82
	ds_write_b32 v103, v82 offset:576
	ds_read_b64 v[88:89], v102 offset:33984
	v_mfma_f32_16x16x4_f32 a[0:3], v82, v48, a[0:3]
	s_waitcnt lgkmcnt(14)
	v_cvt_f32_f64_e32 v83, v[90:91]
	v_mul_f32_e32 v83, v101, v83
	v_fmac_f32_e32 v104, v83, v83
	ds_write_b32 v103, v83 offset:832
	ds_read_b64 v[90:91], v102 offset:34496
	v_mfma_f32_16x16x4_f32 a[4:7], v83, v49, a[4:7]
	s_waitcnt lgkmcnt(14)
	v_cvt_f32_f64_e32 v80, v[92:93]
	v_mul_f32_e32 v80, v101, v80
	v_fmac_f32_e32 v104, v80, v80
	ds_write_b32 v103, v80 offset:80
	ds_read_b64 v[92:93], v102 offset:32992
	v_mfma_f32_16x16x4_f32 a[0:3], v80, v42, a[0:3]
	s_waitcnt lgkmcnt(14)
	v_cvt_f32_f64_e32 v81, v[94:95]
	v_mul_f32_e32 v81, v101, v81
	v_fmac_f32_e32 v104, v81, v81
	ds_write_b32 v103, v81 offset:336
	ds_read_b64 v[94:95], v102 offset:33504
	v_mfma_f32_16x16x4_f32 a[4:7], v81, v43, a[4:7]
	s_waitcnt lgkmcnt(14)
	v_cvt_f32_f64_e32 v82, v[96:97]
	v_mul_f32_e32 v82, v101, v82
	v_fmac_f32_e32 v104, v82, v82
	ds_write_b32 v103, v82 offset:592
	ds_read_b64 v[96:97], v102 offset:34016
	v_mfma_f32_16x16x4_f32 a[0:3], v82, v44, a[0:3]
	s_waitcnt lgkmcnt(14)
	v_cvt_f32_f64_e32 v83, v[98:99]
	v_mul_f32_e32 v83, v101, v83
	v_fmac_f32_e32 v104, v83, v83
	ds_write_b32 v103, v83 offset:848
	ds_read_b64 v[98:99], v102 offset:34528
	v_mfma_f32_16x16x4_f32 a[4:7], v83, v45, a[4:7]
	s_waitcnt lgkmcnt(14)
	v_cvt_f32_f64_e32 v80, v[84:85]
	v_mul_f32_e32 v80, v101, v80
	v_fmac_f32_e32 v104, v80, v80
	ds_write_b32 v103, v80 offset:96
	ds_read_b64 v[84:85], v102 offset:33024
	v_mfma_f32_16x16x4_f32 a[0:3], v80, v38, a[0:3]
	s_waitcnt lgkmcnt(14)
	v_cvt_f32_f64_e32 v81, v[86:87]
	v_mul_f32_e32 v81, v101, v81
	v_fmac_f32_e32 v104, v81, v81
	ds_write_b32 v103, v81 offset:352
	ds_read_b64 v[86:87], v102 offset:33536
	v_mfma_f32_16x16x4_f32 a[4:7], v81, v39, a[4:7]
	s_waitcnt lgkmcnt(14)
	v_cvt_f32_f64_e32 v82, v[88:89]
	v_mul_f32_e32 v82, v101, v82
	v_fmac_f32_e32 v104, v82, v82
	ds_write_b32 v103, v82 offset:608
	ds_read_b64 v[88:89], v102 offset:34048
	v_mfma_f32_16x16x4_f32 a[0:3], v82, v40, a[0:3]
	s_waitcnt lgkmcnt(14)
	v_cvt_f32_f64_e32 v83, v[90:91]
	v_mul_f32_e32 v83, v101, v83
	v_fmac_f32_e32 v104, v83, v83
	ds_write_b32 v103, v83 offset:864
	ds_read_b64 v[90:91], v102 offset:34560
	v_mfma_f32_16x16x4_f32 a[4:7], v83, v41, a[4:7]
	s_waitcnt lgkmcnt(14)
	v_cvt_f32_f64_e32 v80, v[92:93]
	v_mul_f32_e32 v80, v101, v80
	v_fmac_f32_e32 v104, v80, v80
	ds_write_b32 v103, v80 offset:112
	ds_read_b64 v[92:93], v102 offset:33056
	v_mfma_f32_16x16x4_f32 a[0:3], v80, v34, a[0:3]
	s_waitcnt lgkmcnt(14)
	v_cvt_f32_f64_e32 v81, v[94:95]
	v_mul_f32_e32 v81, v101, v81
	v_fmac_f32_e32 v104, v81, v81
	ds_write_b32 v103, v81 offset:368
	ds_read_b64 v[94:95], v102 offset:33568
	v_mfma_f32_16x16x4_f32 a[4:7], v81, v35, a[4:7]
	s_waitcnt lgkmcnt(14)
	v_cvt_f32_f64_e32 v82, v[96:97]
	v_mul_f32_e32 v82, v101, v82
	v_fmac_f32_e32 v104, v82, v82
	ds_write_b32 v103, v82 offset:624
	ds_read_b64 v[96:97], v102 offset:34080
	v_mfma_f32_16x16x4_f32 a[0:3], v82, v36, a[0:3]
	s_waitcnt lgkmcnt(14)
	v_cvt_f32_f64_e32 v83, v[98:99]
	v_mul_f32_e32 v83, v101, v83
	v_fmac_f32_e32 v104, v83, v83
	ds_write_b32 v103, v83 offset:880
	ds_read_b64 v[98:99], v102 offset:34592
	v_mfma_f32_16x16x4_f32 a[4:7], v83, v37, a[4:7]
	s_waitcnt lgkmcnt(14)
	v_cvt_f32_f64_e32 v80, v[84:85]
	v_mul_f32_e32 v80, v101, v80
	v_fmac_f32_e32 v104, v80, v80
	ds_write_b32 v103, v80 offset:128
	ds_read_b64 v[84:85], v102 offset:33088
	v_mfma_f32_16x16x4_f32 a[0:3], v80, v30, a[0:3]
	s_waitcnt lgkmcnt(14)
	v_cvt_f32_f64_e32 v81, v[86:87]
	v_mul_f32_e32 v81, v101, v81
	v_fmac_f32_e32 v104, v81, v81
	ds_write_b32 v103, v81 offset:384
	ds_read_b64 v[86:87], v102 offset:33600
	v_mfma_f32_16x16x4_f32 a[4:7], v81, v31, a[4:7]
	s_waitcnt lgkmcnt(14)
	v_cvt_f32_f64_e32 v82, v[88:89]
	v_mul_f32_e32 v82, v101, v82
	v_fmac_f32_e32 v104, v82, v82
	ds_write_b32 v103, v82 offset:640
	ds_read_b64 v[88:89], v102 offset:34112
	v_mfma_f32_16x16x4_f32 a[0:3], v82, v32, a[0:3]
	s_waitcnt lgkmcnt(14)
	v_cvt_f32_f64_e32 v83, v[90:91]
	v_mul_f32_e32 v83, v101, v83
	v_fmac_f32_e32 v104, v83, v83
	ds_write_b32 v103, v83 offset:896
	ds_read_b64 v[90:91], v102 offset:34624
	v_mfma_f32_16x16x4_f32 a[4:7], v83, v33, a[4:7]
	s_waitcnt lgkmcnt(14)
	v_cvt_f32_f64_e32 v80, v[92:93]
	v_mul_f32_e32 v80, v101, v80
	v_fmac_f32_e32 v104, v80, v80
	ds_write_b32 v103, v80 offset:144
	ds_read_b64 v[92:93], v102 offset:33120
	v_mfma_f32_16x16x4_f32 a[0:3], v80, v26, a[0:3]
	s_waitcnt lgkmcnt(14)
	v_cvt_f32_f64_e32 v81, v[94:95]
	v_mul_f32_e32 v81, v101, v81
	v_fmac_f32_e32 v104, v81, v81
	ds_write_b32 v103, v81 offset:400
	ds_read_b64 v[94:95], v102 offset:33632
	v_mfma_f32_16x16x4_f32 a[4:7], v81, v27, a[4:7]
	s_waitcnt lgkmcnt(14)
	v_cvt_f32_f64_e32 v82, v[96:97]
	v_mul_f32_e32 v82, v101, v82
	v_fmac_f32_e32 v104, v82, v82
	ds_write_b32 v103, v82 offset:656
	ds_read_b64 v[96:97], v102 offset:34144
	v_mfma_f32_16x16x4_f32 a[0:3], v82, v28, a[0:3]
	s_waitcnt lgkmcnt(14)
	v_cvt_f32_f64_e32 v83, v[98:99]
	v_mul_f32_e32 v83, v101, v83
	v_fmac_f32_e32 v104, v83, v83
	ds_write_b32 v103, v83 offset:912
	ds_read_b64 v[98:99], v102 offset:34656
	v_mfma_f32_16x16x4_f32 a[4:7], v83, v29, a[4:7]
	s_waitcnt lgkmcnt(14)
	v_cvt_f32_f64_e32 v80, v[84:85]
	v_mul_f32_e32 v80, v101, v80
	v_fmac_f32_e32 v104, v80, v80
	ds_write_b32 v103, v80 offset:160
	ds_read_b64 v[84:85], v102 offset:33152
	v_mfma_f32_16x16x4_f32 a[0:3], v80, v22, a[0:3]
	s_waitcnt lgkmcnt(14)
	v_cvt_f32_f64_e32 v81, v[86:87]
	v_mul_f32_e32 v81, v101, v81
	v_fmac_f32_e32 v104, v81, v81
	ds_write_b32 v103, v81 offset:416
	ds_read_b64 v[86:87], v102 offset:33664
	v_mfma_f32_16x16x4_f32 a[4:7], v81, v23, a[4:7]
	s_waitcnt lgkmcnt(14)
	v_cvt_f32_f64_e32 v82, v[88:89]
	v_mul_f32_e32 v82, v101, v82
	v_fmac_f32_e32 v104, v82, v82
	ds_write_b32 v103, v82 offset:672
	ds_read_b64 v[88:89], v102 offset:34176
	v_mfma_f32_16x16x4_f32 a[0:3], v82, v24, a[0:3]
	s_waitcnt lgkmcnt(14)
	v_cvt_f32_f64_e32 v83, v[90:91]
	v_mul_f32_e32 v83, v101, v83
	v_fmac_f32_e32 v104, v83, v83
	ds_write_b32 v103, v83 offset:928
	ds_read_b64 v[90:91], v102 offset:34688
	v_mfma_f32_16x16x4_f32 a[4:7], v83, v25, a[4:7]
	s_waitcnt lgkmcnt(14)
	v_cvt_f32_f64_e32 v80, v[92:93]
	v_mul_f32_e32 v80, v101, v80
	v_fmac_f32_e32 v104, v80, v80
	ds_write_b32 v103, v80 offset:176
	ds_read_b64 v[92:93], v102 offset:33184
	v_mfma_f32_16x16x4_f32 a[0:3], v80, v18, a[0:3]
	s_waitcnt lgkmcnt(14)
	v_cvt_f32_f64_e32 v81, v[94:95]
	v_mul_f32_e32 v81, v101, v81
	v_fmac_f32_e32 v104, v81, v81
	ds_write_b32 v103, v81 offset:432
	ds_read_b64 v[94:95], v102 offset:33696
	v_mfma_f32_16x16x4_f32 a[4:7], v81, v19, a[4:7]
	s_waitcnt lgkmcnt(14)
	v_cvt_f32_f64_e32 v82, v[96:97]
	v_mul_f32_e32 v82, v101, v82
	v_fmac_f32_e32 v104, v82, v82
	ds_write_b32 v103, v82 offset:688
	ds_read_b64 v[96:97], v102 offset:34208
	v_mfma_f32_16x16x4_f32 a[0:3], v82, v20, a[0:3]
	s_waitcnt lgkmcnt(14)
	v_cvt_f32_f64_e32 v83, v[98:99]
	v_mul_f32_e32 v83, v101, v83
	v_fmac_f32_e32 v104, v83, v83
	ds_write_b32 v103, v83 offset:944
	ds_read_b64 v[98:99], v102 offset:34720
	v_mfma_f32_16x16x4_f32 a[4:7], v83, v21, a[4:7]
	s_waitcnt lgkmcnt(14)
	v_cvt_f32_f64_e32 v80, v[84:85]
	v_mul_f32_e32 v80, v101, v80
	v_fmac_f32_e32 v104, v80, v80
	ds_write_b32 v103, v80 offset:192
	ds_read_b64 v[84:85], v102 offset:33216
	v_mfma_f32_16x16x4_f32 a[0:3], v80, v14, a[0:3]
	s_waitcnt lgkmcnt(14)
	v_cvt_f32_f64_e32 v81, v[86:87]
	v_mul_f32_e32 v81, v101, v81
	v_fmac_f32_e32 v104, v81, v81
	ds_write_b32 v103, v81 offset:448
	ds_read_b64 v[86:87], v102 offset:33728
	v_mfma_f32_16x16x4_f32 a[4:7], v81, v15, a[4:7]
	s_waitcnt lgkmcnt(14)
	v_cvt_f32_f64_e32 v82, v[88:89]
	v_mul_f32_e32 v82, v101, v82
	v_fmac_f32_e32 v104, v82, v82
	ds_write_b32 v103, v82 offset:704
	ds_read_b64 v[88:89], v102 offset:34240
	v_mfma_f32_16x16x4_f32 a[0:3], v82, v16, a[0:3]
	s_waitcnt lgkmcnt(14)
	v_cvt_f32_f64_e32 v83, v[90:91]
	v_mul_f32_e32 v83, v101, v83
	v_fmac_f32_e32 v104, v83, v83
	ds_write_b32 v103, v83 offset:960
	ds_read_b64 v[90:91], v102 offset:34752
	v_mfma_f32_16x16x4_f32 a[4:7], v83, v17, a[4:7]
	s_waitcnt lgkmcnt(14)
	v_cvt_f32_f64_e32 v80, v[92:93]
	v_mul_f32_e32 v80, v101, v80
	v_fmac_f32_e32 v104, v80, v80
	ds_write_b32 v103, v80 offset:208
	ds_read_b64 v[92:93], v102 offset:33248
	v_mfma_f32_16x16x4_f32 a[0:3], v80, v10, a[0:3]
	s_waitcnt lgkmcnt(14)
	v_cvt_f32_f64_e32 v81, v[94:95]
	v_mul_f32_e32 v81, v101, v81
	v_fmac_f32_e32 v104, v81, v81
	ds_write_b32 v103, v81 offset:464
	ds_read_b64 v[94:95], v102 offset:33760
	v_mfma_f32_16x16x4_f32 a[4:7], v81, v11, a[4:7]
	s_waitcnt lgkmcnt(14)
	v_cvt_f32_f64_e32 v82, v[96:97]
	v_mul_f32_e32 v82, v101, v82
	v_fmac_f32_e32 v104, v82, v82
	ds_write_b32 v103, v82 offset:720
	ds_read_b64 v[96:97], v102 offset:34272
	v_mfma_f32_16x16x4_f32 a[0:3], v82, v12, a[0:3]
	s_waitcnt lgkmcnt(14)
	v_cvt_f32_f64_e32 v83, v[98:99]
	v_mul_f32_e32 v83, v101, v83
	v_fmac_f32_e32 v104, v83, v83
	ds_write_b32 v103, v83 offset:976
	ds_read_b64 v[98:99], v102 offset:34784
	v_mfma_f32_16x16x4_f32 a[4:7], v83, v13, a[4:7]
	s_waitcnt lgkmcnt(14)
	v_cvt_f32_f64_e32 v80, v[84:85]
	v_mul_f32_e32 v80, v101, v80
	v_fmac_f32_e32 v104, v80, v80
	ds_write_b32 v103, v80 offset:224
	v_mfma_f32_16x16x4_f32 a[0:3], v80, v6, a[0:3]
	s_waitcnt lgkmcnt(13)
	v_cvt_f32_f64_e32 v81, v[86:87]
	v_mul_f32_e32 v81, v101, v81
	v_fmac_f32_e32 v104, v81, v81
	ds_write_b32 v103, v81 offset:480
	v_mfma_f32_16x16x4_f32 a[4:7], v81, v7, a[4:7]
	s_waitcnt lgkmcnt(12)
	v_cvt_f32_f64_e32 v82, v[88:89]
	v_mul_f32_e32 v82, v101, v82
	v_fmac_f32_e32 v104, v82, v82
	ds_write_b32 v103, v82 offset:736
	v_mfma_f32_16x16x4_f32 a[0:3], v82, v8, a[0:3]
	s_waitcnt lgkmcnt(11)
	v_cvt_f32_f64_e32 v83, v[90:91]
	v_mul_f32_e32 v83, v101, v83
	v_fmac_f32_e32 v104, v83, v83
	ds_write_b32 v103, v83 offset:992
	v_mfma_f32_16x16x4_f32 a[4:7], v83, v9, a[4:7]
	s_waitcnt lgkmcnt(10)
	v_cvt_f32_f64_e32 v80, v[92:93]
	v_mul_f32_e32 v80, v101, v80
	v_fmac_f32_e32 v104, v80, v80
	ds_write_b32 v103, v80 offset:240
	v_mfma_f32_16x16x4_f32 a[0:3], v80, v2, a[0:3]
	s_waitcnt lgkmcnt(9)
	v_cvt_f32_f64_e32 v81, v[94:95]
	v_mul_f32_e32 v81, v101, v81
	v_fmac_f32_e32 v104, v81, v81
	ds_write_b32 v103, v81 offset:496
	v_mfma_f32_16x16x4_f32 a[4:7], v81, v3, a[4:7]
	s_waitcnt lgkmcnt(8)
	v_cvt_f32_f64_e32 v82, v[96:97]
	v_mul_f32_e32 v82, v101, v82
	v_fmac_f32_e32 v104, v82, v82
	ds_write_b32 v103, v82 offset:752
	v_mfma_f32_16x16x4_f32 a[0:3], v82, v4, a[0:3]
	s_waitcnt lgkmcnt(7)
	v_cvt_f32_f64_e32 v83, v[98:99]
	v_mul_f32_e32 v83, v101, v83
	v_fmac_f32_e32 v104, v83, v83
	ds_write_b32 v103, v83 offset:1008
	v_mfma_f32_16x16x4_f32 a[4:7], v83, v5, a[4:7]
	v_mbcnt_lo_u32_b32 v110, -1, 0
	v_mbcnt_hi_u32_b32 v110, -1, v110
	v_xor_b32_e32 v111, 16, v110
	v_lshlrev_b32_e32 v111, 2, v111
	ds_bpermute_b32 v111, v111, v104
	v_xor_b32_e32 v112, 32, v110
	v_lshlrev_b32_e32 v112, 2, v112
	s_waitcnt lgkmcnt(0)
	v_add_f32_e32 v104, v104, v111
	ds_bpermute_b32 v112, v112, v104
	v_lshlrev_b32_e32 v66, 2, v138
	s_lshl_b32 s0, s24, 2
	s_add_i32 s0, s0, 0x10100
	v_lshlrev_b32_e32 v3, 10, v140
	v_add3_u32 v3, s0, v66, v3
	v_or_b32_e32 v7, s29, v140
	v_lshl_or_b32 v4, v7, 8, v66
	v_add_u32_e32 v4, 0x10100, v4
	s_nop 4
	v_accvgpr_read_b32 v106, a0
	v_accvgpr_read_b32 v107, a1
	v_accvgpr_read_b32 v108, a2
	v_accvgpr_read_b32 v109, a3
	v_accvgpr_read_b32 v113, a4
	v_add_f32_e32 v106, v106, v113
	v_accvgpr_read_b32 v113, a5
	v_add_f32_e32 v107, v107, v113
	v_accvgpr_read_b32 v113, a6
	v_add_f32_e32 v108, v108, v113
	v_accvgpr_read_b32 v113, a7
	v_add_f32_e32 v109, v109, v113
	v_fma_f32 v106, -2.0, v106, v105
	v_fma_f32 v107, -2.0, v107, v105
	v_fma_f32 v108, -2.0, v108, v105
	v_fma_f32 v109, -2.0, v109, v105
	ds_write2st64_b32 v3, v106, v107 offset1:1
	ds_write2st64_b32 v3, v108, v109 offset0:2 offset1:3
	v_mov_b32_e32 v114, 0x11200
	v_lshl_add_u32 v114, v138, 2, v114
	v_cmp_gt_u32_e32 vcc, 16, v1
	s_and_saveexec_b64 s[30:31], vcc
	s_waitcnt lgkmcnt(0)
	v_add_f32_e32 v104, v104, v112
	ds_write_b32 v114, v104
	s_mov_b64 exec, s[30:31]
	s_waitcnt lgkmcnt(0)
	s_barrier
	ds_read2_b32 v[2:3], v4 offset1:16
	ds_read2_b32 v[4:5], v4 offset0:32 offset1:48
	v_or_b32_e32 v6, 16, v138
	v_or_b32_e32 v8, 32, v138
	v_or_b32_e32 v9, 48, v138
	s_waitcnt lgkmcnt(1)
	v_cmp_lt_f32_e32 vcc, v3, v2
	s_nop 1
	v_cndmask_b32_e32 v10, v2, v3, vcc
	v_cndmask_b32_e32 v6, v138, v6, vcc
	s_waitcnt lgkmcnt(0)
	v_cmp_lt_f32_e32 vcc, v4, v10
	s_nop 1
	v_cndmask_b32_e32 v10, v10, v4, vcc
	v_cndmask_b32_e32 v8, v6, v8, vcc
	v_cmp_lt_f32_e32 vcc, v5, v10
	s_nop 1
	v_cndmask_b32_e32 v6, v10, v5, vcc
	v_cndmask_b32_e32 v14, v8, v9, vcc
	s_nop 0
	v_mov_b32_dpp v9, v6 quad_perm:[1,0,3,2] row_mask:0xf bank_mask:0xf bound_ctrl:1
	v_mov_b32_dpp v8, v14 quad_perm:[1,0,3,2] row_mask:0xf bank_mask:0xf bound_ctrl:1
	v_cmp_gt_f32_e64 s[4:5], v6, v9
	v_cmp_ngt_f32_e32 vcc, v6, v9
	s_and_saveexec_b64 s[6:7], vcc
	v_cmp_eq_f32_e32 vcc, v6, v9
	v_cmp_lt_i32_e64 s[0:1], v8, v14
	s_and_b64 s[0:1], vcc, s[0:1]
	s_andn2_b64 s[4:5], s[4:5], exec
	s_and_b64 s[0:1], s[0:1], exec
	s_or_b64 s[4:5], s[4:5], s[0:1]
	s_or_b64 exec, exec, s[6:7]
	s_and_saveexec_b64 s[0:1], s[4:5]
	v_mov_b32_e32 v6, v9
	v_mov_b32_e32 v14, v8
	s_or_b64 exec, exec, s[0:1]
	v_mov_b32_dpp v9, v6 quad_perm:[2,3,0,1] row_mask:0xf bank_mask:0xf bound_ctrl:1
	v_mov_b32_dpp v8, v14 quad_perm:[2,3,0,1] row_mask:0xf bank_mask:0xf bound_ctrl:1
	v_cmp_gt_f32_e64 s[4:5], v6, v9
	v_cmp_ngt_f32_e32 vcc, v6, v9
	s_and_saveexec_b64 s[6:7], vcc
	v_cmp_eq_f32_e32 vcc, v6, v9
	v_cmp_lt_i32_e64 s[0:1], v8, v14
	s_and_b64 s[0:1], vcc, s[0:1]
	s_andn2_b64 s[4:5], s[4:5], exec
	s_and_b64 s[0:1], s[0:1], exec
	s_or_b64 s[4:5], s[4:5], s[0:1]
	s_or_b64 exec, exec, s[6:7]
	s_and_saveexec_b64 s[0:1], s[4:5]
	v_mov_b32_e32 v6, v9
	v_mov_b32_e32 v14, v8
	s_or_b64 exec, exec, s[0:1]
	v_mov_b32_dpp v9, v6 row_half_mirror row_mask:0xf bank_mask:0xf bound_ctrl:1
	v_mov_b32_dpp v8, v14 row_half_mirror row_mask:0xf bank_mask:0xf bound_ctrl:1
	v_cmp_gt_f32_e64 s[4:5], v6, v9
	v_cmp_ngt_f32_e32 vcc, v6, v9
	s_and_saveexec_b64 s[6:7], vcc
	v_cmp_eq_f32_e32 vcc, v6, v9
	v_cmp_lt_i32_e64 s[0:1], v8, v14
	s_and_b64 s[0:1], vcc, s[0:1]
	s_andn2_b64 s[4:5], s[4:5], exec
	s_and_b64 s[0:1], s[0:1], exec
	s_or_b64 s[4:5], s[4:5], s[0:1]
	s_or_b64 exec, exec, s[6:7]
	s_and_saveexec_b64 s[0:1], s[4:5]
	v_mov_b32_e32 v6, v9
	v_mov_b32_e32 v14, v8
	s_or_b64 exec, exec, s[0:1]
	v_mov_b32_dpp v8, v6 row_mirror row_mask:0xf bank_mask:0xf bound_ctrl:1
	v_mov_b32_dpp v9, v14 row_mirror row_mask:0xf bank_mask:0xf bound_ctrl:1
	v_cmp_gt_f32_e64 s[4:5], v6, v8
	v_cmp_ngt_f32_e32 vcc, v6, v8
	s_and_saveexec_b64 s[6:7], vcc
	v_cmp_eq_f32_e32 vcc, v6, v8
	v_cmp_lt_i32_e64 s[0:1], v9, v14
	s_and_b64 s[0:1], vcc, s[0:1]
	s_andn2_b64 s[4:5], s[4:5], exec
	s_and_b64 s[0:1], s[0:1], exec
	s_or_b64 s[4:5], s[4:5], s[0:1]
	s_or_b64 exec, exec, s[6:7]
	s_and_saveexec_b64 s[0:1], s[4:5]
	v_mov_b32_e32 v6, v8
	v_mov_b32_e32 v14, v9
	s_or_b64 exec, exec, s[0:1]
	v_mov_b32_e32 v8, 0x11300
	v_lshl_or_b32 v8, v1, 2, v8
	ds_read_b32 v8, v8
	v_mov_b32_e32 v9, 0x11200
	v_lshl_add_u32 v7, v7, 2, v9
	ds_read_b32 v9, v7
	v_mov_b32_e32 v13, 0x260
	s_waitcnt lgkmcnt(1)
	v_mov_b32_dpp v7, v8 quad_perm:[1,0,3,2] row_mask:0xf bank_mask:0xf bound_ctrl:1
	v_max_f32_e32 v8, v8, v8
	v_max_f32_e32 v7, v7, v7
	v_max_f32_e32 v7, v8, v7
	v_lshlrev_b32_e32 v18, 2, v139
	v_mov_b32_e32 v19, 0
	v_mov_b32_dpp v8, v7 quad_perm:[2,3,0,1] row_mask:0xf bank_mask:0xf bound_ctrl:1
	v_max_f32_e32 v8, v8, v8
	v_max_f32_e32 v7, v7, v8
	s_mov_b32 s25, 0
	s_mov_b32 s26, s25
	v_mov_b32_dpp v8, v7 row_half_mirror row_mask:0xf bank_mask:0xf bound_ctrl:1
	v_max_f32_e32 v8, v8, v8
	v_max_f32_e32 v7, v7, v8
	s_nop 1
	v_mov_b32_dpp v8, v7 row_mirror row_mask:0xf bank_mask:0xf bound_ctrl:1
	v_max_f32_e32 v8, v8, v8
	v_max_f32_e32 v7, v7, v8
	s_nop 0
	v_readlane_b32 s4, v7, 32
	v_readlane_b32 s5, v7, 48
	v_readlane_b32 s0, v7, 0
	v_readlane_b32 s1, v7, 16
	v_max_f32_e64 v7, s5, s5
	v_max_f32_e64 v8, s4, s4
	v_max_f32_e32 v7, v8, v7
	v_mov_b32_e32 v8, s1
	v_max3_f32 v8, s0, v8, v7
	s_mov_b32 s0, 0x3f800347
	s_mov_b32 s1, 0x3f8020c5
	s_waitcnt lgkmcnt(0)
	v_pk_mul_f32 v[8:9], v[8:9], s[0:1]
	s_mov_b32 s4, 0xf800000
	v_mul_f32_e32 v7, 0x4f800000, v9
	v_cmp_gt_f32_e32 vcc, s4, v9
	s_nop 1
	v_cndmask_b32_e32 v7, v9, v7, vcc
	v_sqrt_f32_e32 v10, v7
	s_nop 0
	v_add_u32_e32 v11, -1, v10
	v_fma_f32 v12, -v11, v10, v7
	v_cmp_ge_f32_e64 s[0:1], 0, v12
	v_add_u32_e32 v12, 1, v10
	s_nop 0
	v_cndmask_b32_e64 v11, v10, v11, s[0:1]
	v_fma_f32 v10, -v12, v10, v7
	v_cmp_lt_f32_e64 s[0:1], 0, v10
	s_nop 1
	v_cndmask_b32_e64 v10, v11, v12, s[0:1]
	v_mul_f32_e32 v11, 0x37800000, v10
	v_cndmask_b32_e32 v10, v10, v11, vcc
	v_mul_f32_e32 v11, 0x4f800000, v8
	v_cmp_gt_f32_e32 vcc, s4, v8
	v_cmp_class_f32_e64 s[0:1], v7, v13
	s_nop 0
	v_cndmask_b32_e32 v11, v8, v11, vcc
	v_sqrt_f32_e32 v12, v11
	v_cndmask_b32_e64 v7, v10, v7, s[0:1]
	v_add_u32_e32 v10, -1, v12
	v_fma_f32 v15, -v10, v12, v11
	v_cmp_ge_f32_e64 s[0:1], 0, v15
	v_add_u32_e32 v15, 1, v12
	s_nop 0
	v_cndmask_b32_e64 v10, v12, v10, s[0:1]
	v_fma_f32 v12, -v15, v12, v11
	v_cmp_lt_f32_e64 s[0:1], 0, v12
	s_nop 1
	v_cndmask_b32_e64 v10, v10, v15, s[0:1]
	v_mul_f32_e32 v12, 0x37800000, v10
	v_cndmask_b32_e32 v10, v10, v12, vcc
	v_cmp_class_f32_e32 vcc, v11, v13
	s_mov_b32 s0, 0x380637bd
	s_mov_b32 s1, 0x350637bd
	v_cndmask_b32_e32 v10, v10, v11, vcc
	v_mul_f32_e32 v7, v7, v10
	v_mul_f32_e32 v7, 0x3f800347, v7
	v_pk_mul_f32 v[8:9], v[8:9], s[0:1]
	s_nop 0
	v_fmamk_f32 v7, v7, 0x3888509c, v9
	v_add_f32_e32 v7, v8, v7
	v_add_f32_e32 v7, 0xda24260, v7
	v_add_f32_e32 v6, v6, v7
	v_cmp_le_f32_e64 s[8:9], v2, v6
	v_cmp_le_f32_e64 s[6:7], v3, v6
	v_cmp_le_f32_e64 s[4:5], v4, v6
	v_lshl_add_u64 v[2:3], s[22:23], 0, v[18:19]
	s_and_b32 s19, s8, 0xffff
	s_lshl_b32 s22, s6, 16
	v_cmp_le_f32_e64 s[0:1], v5, v6
	s_or_b32 s24, s19, s22
	s_and_b32 s23, s4, 0xffff
	s_mov_b32 s22, s25
	s_or_b64 s[22:23], s[24:25], s[22:23]
	s_lshl_b32 s27, s0, 16
	s_or_b64 s[26:27], s[22:23], s[26:27]
	s_add_u32 s22, s26, -1
	s_addc_u32 s23, s27, -1
	s_and_b64 s[22:23], s[26:27], s[22:23]
	s_cmp_eq_u64 s[22:23], 0
	v_readlane_b32 s22, v14, 0
	s_cbranch_scc1 .LBB0_139
	s_lshl_b32 s19, s29, 2
	s_add_i32 s19, s19, 0x11100
	v_mov_b32_e32 v4, s19
	ds_read_b32 v4, v4
	s_mul_i32 s19, s17, 0x2040
	v_add_u32_e32 v8, s19, v135
	v_mov_b32_e32 v15, 0x7f800000
	s_waitcnt lgkmcnt(0)
	v_max_i32_e32 v4, 1, v4
	v_cvt_f64_u32_e32 v[12:13], v4
	v_div_scale_f64 v[16:17], s[30:31], v[12:13], v[12:13], 1.0
	v_rcp_f64_e32 v[20:21], v[16:17]
	v_div_scale_f64 v[22:23], vcc, 1.0, v[12:13], 1.0
	ds_read2st64_b64 v[4:7], v8 offset0:64 offset1:65
	ds_read2st64_b64 v[8:11], v8 offset0:66 offset1:67
	v_fma_f64 v[24:25], -v[16:17], v[20:21], 1.0
	v_fmac_f64_e32 v[20:21], v[20:21], v[24:25]
	v_fma_f64 v[24:25], -v[16:17], v[20:21], 1.0
	v_fmac_f64_e32 v[20:21], v[20:21], v[24:25]
	v_mul_f64 v[24:25], v[22:23], v[20:21]
	v_fma_f64 v[16:17], -v[16:17], v[24:25], v[22:23]
	v_div_fmas_f64 v[16:17], v[16:17], v[20:21], v[24:25]
	v_div_fixup_f64 v[12:13], v[16:17], v[12:13], 1.0
	s_waitcnt lgkmcnt(1)
	v_mul_f64 v[6:7], v[6:7], v[12:13]
	v_mul_f64 v[4:5], v[4:5], v[12:13]
	s_waitcnt lgkmcnt(0)
	v_mul_f64 v[8:9], v[8:9], v[12:13]
	v_mul_f64 v[10:11], v[12:13], v[10:11]
	v_mul_f64 v[12:13], v[6:7], v[6:7]
	v_fmac_f64_e32 v[12:13], v[4:5], v[4:5]
	v_fmac_f64_e32 v[12:13], v[8:9], v[8:9]
	v_fmac_f64_e32 v[12:13], v[10:11], v[10:11]
	s_nop 1
	v_mov_b32_dpp v16, v12 quad_perm:[1,0,3,2] row_mask:0xf bank_mask:0xf bound_ctrl:1
	v_mov_b32_dpp v17, v13 quad_perm:[1,0,3,2] row_mask:0xf bank_mask:0xf bound_ctrl:1
	v_add_f64 v[12:13], v[12:13], v[16:17]
	s_nop 1
	v_mov_b32_dpp v16, v12 quad_perm:[2,3,0,1] row_mask:0xf bank_mask:0xf bound_ctrl:1
	v_mov_b32_dpp v17, v13 quad_perm:[2,3,0,1] row_mask:0xf bank_mask:0xf bound_ctrl:1
	v_add_f64 v[12:13], v[12:13], v[16:17]
	s_nop 1
	v_mov_b32_dpp v16, v12 row_half_mirror row_mask:0xf bank_mask:0xf bound_ctrl:1
	v_mov_b32_dpp v17, v13 row_half_mirror row_mask:0xf bank_mask:0xf bound_ctrl:1
	v_add_f64 v[12:13], v[12:13], v[16:17]
	s_nop 1
	v_mov_b32_dpp v16, v12 row_mirror row_mask:0xf bank_mask:0xf bound_ctrl:1
	v_mov_b32_dpp v17, v13 row_mirror row_mask:0xf bank_mask:0xf bound_ctrl:1
	v_add_f64 v[12:13], v[12:13], v[16:17]
	s_nop 0
	v_readlane_b32 s19, v13, 16
	v_readlane_b32 s23, v12, 16
	v_readlane_b32 s31, v13, 0
	v_readlane_b32 s30, v12, 0
	v_mov_b32_e32 v16, s23
	v_mov_b32_e32 v17, s19
	v_readlane_b32 s19, v13, 48
	v_readlane_b32 s23, v12, 48
	v_add_f64 v[16:17], s[30:31], v[16:17]
	v_readlane_b32 s31, v13, 32
	v_readlane_b32 s30, v12, 32
	v_mov_b32_e32 v12, s23
	v_mov_b32_e32 v13, s19
	v_add_f64 v[12:13], s[30:31], v[12:13]
	v_add_f64 v[12:13], v[16:17], v[12:13]
